# speedup vs baseline: 1.0253x; 1.0015x over previous
.Lj_norr:
	s_or_b64 exec, exec, s[10:11]
	s_waitcnt lgkmcnt(0)
	v_and_b32_e32 v240, v240, v241
	v_and_b32_e32 v242, v242, v243
	v_and_b32_e32 v240, v240, v242
	s_nop 0
	v_readfirstlane_b32 s83, v240
	s_cmp_lt_u32 s20, 2
	s_cbranch_scc1 .Lj_nostop
	s_cmp_eq_u32 s83, 0
	s_cbranch_scc0 .Lj_stop
.Lj_nostop:
	v_mov_b64_e32 v[146:147], 0
	v_mov_b64_e32 v[148:149], 0
	v_mov_b64_e32 v[154:155], 0
	v_mov_b64_e32 v[156:157], 0
	v_mov_b64_e32 v[158:159], 0
	v_mov_b64_e32 v[160:161], 0
	v_mov_b64_e32 v[162:163], 0
	v_mov_b64_e32 v[164:165], 0
	v_mov_b32_e32 v231, 0
	s_lshl_b32 s10, s70, 13
	s_add_i32 s14, s10, s34
	s_mov_b32 s15, 0
	v_lshl_add_u64 v[244:245], v[192:193], 0, s[14:15]
	s_add_i32 s14, s10, s30
	v_lshl_add_u64 v[246:247], v[192:193], 0, s[14:15]
	s_add_i32 s14, s10, s28
	v_lshl_add_u64 v[248:249], v[192:193], 0, s[14:15]
	v_smfmac_f32_16x16x64_bf16 v[162:165], v[150:153], v[166:173], v223
	ds_read_b128 v[166:169], v224 offset:6144
	v_smfmac_f32_16x16x64_bf16 v[146:149], v[150:153], v[2:9], v223
	ds_read_b128 v[170:173], v224 offset:7168
	v_smfmac_f32_16x16x64_bf16 v[154:157], v[150:153], v[18:25], v223
	v_smfmac_f32_16x16x64_bf16 v[158:161], v[150:153], v[34:41], v223
	s_cmp_eq_u32 s20, 0
	s_cbranch_scc1 .Lj_nopoll0
	global_load_dwordx2 v[204:205], v[244:245], off sc1
	global_load_dwordx2 v[202:203], v[246:247], off sc1
	global_load_dwordx2 v[218:219], v[248:249], off sc1
.Lj_nopoll0:
	v_smfmac_f32_16x16x64_bf16 v[162:165], v[194:197], v[174:181], v223
	ds_read_b128 v[174:177], v224 offset:8192
	v_smfmac_f32_16x16x64_bf16 v[146:149], v[194:197], v[10:17], v223
	ds_read_b128 v[178:181], v224 offset:9216
	v_smfmac_f32_16x16x64_bf16 v[154:157], v[194:197], v[26:33], v223
	v_smfmac_f32_16x16x64_bf16 v[158:161], v[194:197], v[42:49], v223
	v_smfmac_f32_16x16x64_bf16 v[162:165], v[198:201], v[182:189], v223
	ds_read_b128 v[182:185], v224 offset:10240
	v_smfmac_f32_16x16x64_bf16 v[146:149], v[198:201], v[50:57], v223
	ds_read_b128 v[186:189], v224 offset:11264
	v_smfmac_f32_16x16x64_bf16 v[154:157], v[198:201], v[66:73], v223
	v_smfmac_f32_16x16x64_bf16 v[158:161], v[198:201], v[82:89], v223
	s_waitcnt lgkmcnt(4)
	v_smfmac_f32_16x16x64_bf16 v[162:165], v[232:235], v[166:173], v223
	ds_read_b128 v[166:169], v224 offset:12288
	v_smfmac_f32_16x16x64_bf16 v[146:149], v[232:235], v[58:65], v223
	ds_read_b128 v[170:173], v224 offset:13312
	v_smfmac_f32_16x16x64_bf16 v[154:157], v[232:235], v[74:81], v223
	v_smfmac_f32_16x16x64_bf16 v[158:161], v[232:235], v[90:97], v223
	s_cmp_eq_u32 s20, 0
	s_cbranch_scc1 .Lj_gdone
	s_mov_b32 s29, 0

.Lj_gdone:
	s_waitcnt lgkmcnt(0)
	s_barrier
	v_add_u32_e32 v240, s45, v229
	v_add_u32_e32 v241, s44, v229
	v_add_u32_e32 v242, s60, v229
	ds_read_b128 v[150:153], v240 offset:0
	ds_read_b128 v[194:197], v240 offset:128
	ds_read_b128 v[198:201], v240 offset:256
	ds_read_b128 v[232:235], v240 offset:384
	s_cmp_eq_u32 s20, 0
	s_cselect_b64 s[36:37], -1, 0
	s_add_i32 s29, s20, 1
	s_and_b32 s14, s29, 1
	s_lshl_b32 s10, s14, 13
	s_mov_b32 s11, 0
	v_lshl_add_u64 v[250:251], v[0:1], 0, s[10:11]
	s_mul_i32 s15, s14, 0x1100
	v_add_u32_e32 v243, s15, v228
	v_mov_b32_e32 v253, s29
	s_waitcnt lgkmcnt(3)
	v_smfmac_f32_16x16x64_bf16 v[162:165], v[150:153], v[174:181], v223
	ds_read_b128 v[174:177], v224 offset:14336
	v_smfmac_f32_16x16x64_bf16 v[146:149], v[150:153], v[98:105], v223
	ds_read_b128 v[178:181], v224 offset:15360
	v_smfmac_f32_16x16x64_bf16 v[154:157], v[150:153], v[114:121], v223
	v_or3_b32 v231, v236, v237, v216
	v_smfmac_f32_16x16x64_bf16 v[158:161], v[150:153], v[130:137], v223
	v_or3_b32 v231, v244, v245, v231
	ds_read_b128 v[150:153], v241 offset:0
	s_waitcnt lgkmcnt(5)
	v_smfmac_f32_16x16x64_bf16 v[162:165], v[194:197], v[182:189], v223
	ds_read_b128 v[182:185], v224 offset:16384
	v_smfmac_f32_16x16x64_bf16 v[146:149], v[194:197], v[106:113], v223
	ds_read_b128 v[186:189], v224 offset:17408
	v_smfmac_f32_16x16x64_bf16 v[154:157], v[194:197], v[122:129], v223
	v_or3_b32 v231, v246, v247, v231
	v_smfmac_f32_16x16x64_bf16 v[158:161], v[194:197], v[138:145], v223
	v_and_b32_e32 v231, 0x7fff7fff, v231
	ds_read_b128 v[194:197], v241 offset:128
	s_waitcnt lgkmcnt(7)
	v_smfmac_f32_16x16x64_bf16 v[162:165], v[198:201], v[166:173], v223
	ds_read_b128 v[166:169], v224 offset:18432
	v_smfmac_f32_16x16x64_bf16 v[146:149], v[198:201], a[0:7], v223
	ds_read_b128 v[170:173], v224 offset:19456
	v_smfmac_f32_16x16x64_bf16 v[154:157], v[198:201], a[16:23], v223
	v_cmp_eq_u32_e32 vcc, 0, v231
	v_smfmac_f32_16x16x64_bf16 v[158:161], v[198:201], a[32:39], v223
	s_lshl_b32 s83, s70, 4
	ds_read_b128 v[198:201], v241 offset:256
	s_waitcnt lgkmcnt(7)
	v_smfmac_f32_16x16x64_bf16 v[162:165], v[232:235], v[174:181], v223
	ds_read_b128 v[174:177], v224 offset:20480
	v_smfmac_f32_16x16x64_bf16 v[146:149], v[232:235], a[8:15], v223
	ds_read_b128 v[178:181], v224 offset:21504
	v_smfmac_f32_16x16x64_bf16 v[154:157], v[232:235], a[24:31], v223
	s_cmp_eq_u64 vcc, exec
	v_smfmac_f32_16x16x64_bf16 v[158:161], v[232:235], a[40:47], v223
	s_cselect_b32 s82, 1, 0
	ds_read_b128 v[232:235], v241 offset:384
	s_waitcnt lgkmcnt(7)
	v_smfmac_f32_16x16x64_bf16 v[162:165], v[150:153], v[182:189], v223
	ds_read_b128 v[182:185], v224 offset:22528
	v_smfmac_f32_16x16x64_bf16 v[146:149], v[150:153], a[48:55], v223
	ds_read_b128 v[186:189], v224 offset:23552
	v_smfmac_f32_16x16x64_bf16 v[154:157], v[150:153], a[64:71], v223
	v_mov_b32_e32 v238, s82
	v_smfmac_f32_16x16x64_bf16 v[158:161], v[150:153], a[80:87], v223
	v_add_u32_e32 v239, s83, v254
	ds_read_b128 v[150:153], v242 offset:0
	s_waitcnt lgkmcnt(7)
	v_smfmac_f32_16x16x64_bf16 v[162:165], v[194:197], v[166:173], v223
	ds_read_b128 v[166:169], v224 offset:24576
	v_smfmac_f32_16x16x64_bf16 v[146:149], v[194:197], a[56:63], v223
	ds_read_b128 v[170:173], v224 offset:25600
	v_smfmac_f32_16x16x64_bf16 v[154:157], v[194:197], a[72:79], v223
	v_smfmac_f32_16x16x64_bf16 v[158:161], v[194:197], a[88:95], v223
	ds_write_b32 v239, v238
	ds_read_b128 v[194:197], v242 offset:128
	s_waitcnt lgkmcnt(8)
	v_smfmac_f32_16x16x64_bf16 v[162:165], v[198:201], v[174:181], v223
	ds_read_b128 v[174:177], v224 offset:26624
	v_smfmac_f32_16x16x64_bf16 v[146:149], v[198:201], a[96:103], v223
	ds_read_b128 v[178:181], v224 offset:27648
	v_smfmac_f32_16x16x64_bf16 v[154:157], v[198:201], a[112:119], v223
	v_smfmac_f32_16x16x64_bf16 v[158:161], v[198:201], a[128:135], v223
	ds_read_b128 v[198:201], v242 offset:256
	s_waitcnt lgkmcnt(8)
	v_smfmac_f32_16x16x64_bf16 v[162:165], v[232:235], v[182:189], v223
	ds_read_b128 v[182:185], v224 offset:28672
	v_smfmac_f32_16x16x64_bf16 v[146:149], v[232:235], a[104:111], v223
	ds_read_b128 v[186:189], v224 offset:29696
	v_smfmac_f32_16x16x64_bf16 v[154:157], v[232:235], a[120:127], v223
	v_smfmac_f32_16x16x64_bf16 v[158:161], v[232:235], a[136:143], v223
	ds_read_b128 v[232:235], v242 offset:384
	s_waitcnt lgkmcnt(8)
	v_smfmac_f32_16x16x64_bf16 v[162:165], v[150:153], v[166:173], v223
	ds_read_b128 v[166:169], v224 offset:30720
	v_smfmac_f32_16x16x64_bf16 v[146:149], v[150:153], a[144:151], v223
	ds_read_b128 v[170:173], v224 offset:31744
	v_smfmac_f32_16x16x64_bf16 v[154:157], v[150:153], a[160:167], v223
	v_smfmac_f32_16x16x64_bf16 v[158:161], v[150:153], a[176:183], v223
	s_waitcnt lgkmcnt(6)
	v_smfmac_f32_16x16x64_bf16 v[162:165], v[194:197], v[174:181], v223
	ds_read_b128 v[174:177], v224 offset:2048
	v_smfmac_f32_16x16x64_bf16 v[146:149], v[194:197], a[152:159], v223
	ds_read_b128 v[178:181], v224 offset:3072
	v_smfmac_f32_16x16x64_bf16 v[154:157], v[194:197], a[168:175], v223
	v_smfmac_f32_16x16x64_bf16 v[158:161], v[194:197], a[184:191], v223
	s_waitcnt lgkmcnt(5)
	v_smfmac_f32_16x16x64_bf16 v[162:165], v[198:201], v[182:189], v223
	ds_read_b128 v[182:185], v224 offset:4096
	v_smfmac_f32_16x16x64_bf16 v[146:149], v[198:201], a[192:199], v223
	ds_read_b128 v[186:189], v224 offset:5120
	v_smfmac_f32_16x16x64_bf16 v[154:157], v[198:201], a[208:215], v223
	v_smfmac_f32_16x16x64_bf16 v[158:161], v[198:201], a[224:231], v223
	s_waitcnt lgkmcnt(4)
	v_smfmac_f32_16x16x64_bf16 v[162:165], v[232:235], v[166:173], v223
	ds_read_b128 v[166:169], v224 offset:0
	v_smfmac_f32_16x16x64_bf16 v[146:149], v[232:235], a[200:207], v223
	ds_read_b128 v[170:173], v224 offset:1024
	v_smfmac_f32_16x16x64_bf16 v[154:157], v[232:235], a[216:223], v223
	v_smfmac_f32_16x16x64_bf16 v[158:161], v[232:235], a[232:239], v223
	s_nop 5
	v_pk_add_f32 v[244:245], v[162:163], v[164:165]
	v_pk_add_f32 v[236:237], v[146:147], v[148:149]
	v_pk_add_f32 v[238:239], v[154:155], v[156:157]
	v_pk_add_f32 v[240:241], v[158:159], v[160:161]
	v_add_f32_e32 v236, v236, v237
	v_add_f32_e32 v237, v238, v239
	v_add_f32_e32 v238, v240, v241
	v_add_f32_e32 v239, v244, v245
	v_cndmask_b32_e64 v236, v236, v237, s[4:5]
	v_cndmask_b32_e64 v236, v236, v238, s[6:7]
	v_cndmask_b32_e64 v156, v236, v239, s[74:75]
	v_add_f32_e32 v236, v208, v156
	v_cndmask_b32_e64 v252, v156, v236, s[36:37]
	global_store_dwordx2 v[250:251], v[252:253], off sc1
	v_cvt_pk_bf16_f32 v237, v252, v252
	v_lshlrev_b32_e32 v238, 16, v237
	v_sub_f32_e32 v238, v252, v238
	v_cvt_pk_bf16_f32 v238, v238, v238
	ds_write_b16 v243, v237
	ds_write_b16 v243, v238 offset:2176
	v_or_b32_e32 v216, v237, v238
	s_cmp_eq_u32 s20, 0
	s_cbranch_scc1 .Lj_nores
	v_mul_f32_e32 v146, v207, v156
	v_mul_f32_e32 v147, v146, v146
	s_nop 1
	v_mov_b32_dpp v147, v147 row_shr:1 row_mask:0xf bank_mask:0xf bound_ctrl:1
	v_fmac_f32_e32 v147, v146, v146
	s_nop 1
	v_add_f32_dpp v146, v147, v147 row_shr:2 row_mask:0xf bank_mask:0xf bound_ctrl:1
	v_mov_b32_e32 v147, v191
	s_nop 0
	v_add_f32_dpp v146, v146, v146 row_shr:4 row_mask:0xf bank_mask:0xf bound_ctrl:1
	s_nop 1
	v_add_f32_dpp v146, v146, v146 row_shr:8 row_mask:0xf bank_mask:0xf bound_ctrl:1
	s_nop 1
	v_mov_b32_dpp v147, v146 row_bcast:15 row_mask:0xa bank_mask:0xf
	v_add_f32_e32 v146, v146, v147
	v_mov_b32_e32 v147, v191
	s_nop 1
	v_mov_b32_dpp v147, v146 row_bcast:31 row_mask:0xc bank_mask:0xf
	s_and_saveexec_b64 s[10:11], s[8:9]
	s_lshl_b32 s14, s14, 4
	s_add_i32 s14, s42, s14
	v_add_f32_e32 v146, v146, v147
	v_mov_b32_e32 v147, s14
	ds_write_b32 v147, v146
	s_or_b64 exec, exec, s[10:11]
